# speedup vs baseline: 1.0033x; 1.0033x over previous
.LBB2_15:
	s_load_dwordx2 s[6:7], s[0:1], 0x30
	s_lshr_b32 s2, s14, 6
	s_mul_i32 s10, s9, 3
	s_mul_i32 s15, s15, 3
	v_lshlrev_b32_e32 v102, 2, v98
	s_lshr_b32 s4, s10, 1
	s_lshl_b32 s2, s2, 4
	v_lshl_or_b32 v103, s8, 6, v1
	s_add_i32 s5, s4, s15
	v_and_or_b32 v1, s2, 16, v102
	s_waitcnt lgkmcnt(0)
	s_barrier
	s_cmp_lt_u32 s5, 32
	v_lshlrev_b32_e32 v98, 3, v1
	v_mov_b32_e32 v99, 0
	s_cselect_b64 s[8:9], -1, 0
	s_cmp_lt_u32 s5, 16
	s_waitcnt lgkmcnt(0)
	v_lshl_add_u64 v[100:101], s[6:7], 0, v[98:99]
	v_or_b32_e32 v98, s12, v103
	s_cselect_b64 s[2:3], -1, 0
	s_cmp_gt_u32 s5, 31
	v_ashrrev_i32_e32 v99, 31, v98
	s_cbranch_scc1 .LBB2_17
	v_lshlrev_b64 v[104:105], 8, v[98:99]
	v_lshl_add_u64 v[108:109], v[100:101], 0, v[104:105]
	global_load_dwordx4 v[104:107], v[108:109], off
	s_nop 0
	global_load_dwordx4 v[108:111], v[108:109], off offset:16
	s_mov_b32 s14, 0x3e38aa3b
	s_waitcnt vmcnt(0)
	v_mov_b32_e32 v113, v106
	v_mov_b32_e32 v106, v105
	v_mov_b32_e32 v105, v110
	v_mov_b32_e32 v110, v109
	v_mov_b32_e32 v112, v104
	v_mov_b32_e32 v104, v108
	v_mul_f32_e32 v108, v94, v106
	v_mul_f32_e32 v109, v95, v107
	v_mul_f32_e32 v106, v90, v106
	v_mul_f32_e32 v107, v91, v107
	v_mul_f32_e32 v114, v96, v110
	v_mul_f32_e32 v115, v97, v111
	v_mul_f32_e32 v110, v92, v110
	v_mul_f32_e32 v111, v93, v111
	v_fma_f32 v90, v90, v112, v108
	v_fma_f32 v91, v91, v113, v109
	v_fma_f32 v94, v94, v112, -v106
	v_fma_f32 v95, v95, v113, -v107
	v_fma_f32 v92, v92, v104, v114
	v_fma_f32 v93, v93, v105, v115
	v_fma_f32 v96, v96, v104, -v110
	v_fma_f32 v97, v97, v105, -v111
	s_cmp_lg_u64 s[2:3], 0
	s_cbranch_scc0 .Lqs_skip_0
	v_mul_f32_e32 v94, s14, v94
	v_mul_f32_e32 v95, s14, v95
	v_mul_f32_e32 v96, s14, v96
	v_mul_f32_e32 v97, s14, v97
	v_mul_f32_e32 v90, s14, v90
	v_mul_f32_e32 v91, s14, v91
	v_mul_f32_e32 v92, s14, v92
	v_mul_f32_e32 v93, s14, v93
.Lqs_skip_0:
.LBB2_17:
	s_lshl_b32 s4, s4, 7
	s_add_i32 s4, s4, 0
	v_lshl_add_u32 v104, v1, 1, s4
	v_cvt_pk_f16_f32 v97, v96, v97
	v_cvt_pk_f16_f32 v96, v94, v95
	v_cvt_pk_f16_f32 v94, v90, v91
	s_movk_i32 s4, 0x190
	v_or_b32_e32 v90, 16, v103
	v_mul_lo_u32 v1, v103, s4
	v_cndmask_b32_e64 v91, 0, 1, s[8:9]
	v_or_b32_e32 v90, s12, v90
	v_cvt_pk_f16_f32 v95, v92, v93
	v_add_u32_e32 v92, v104, v1
	v_cmp_ne_u32_e64 s[4:5], 1, v91
	s_andn2_b64 vcc, exec, s[8:9]
	v_ashrrev_i32_e32 v91, 31, v90
	ds_write2_b64 v92, v[96:97], v[94:95] offset1:8
	s_cbranch_vccnz .LBB2_19
	v_lshlrev_b64 v[94:95], 8, v[90:91]
	v_lshl_add_u64 v[104:105], v[100:101], 0, v[94:95]
	global_load_dwordx4 v[94:97], v[104:105], off
	s_nop 0
	global_load_dwordx4 v[104:107], v[104:105], off offset:16
	s_mov_b32 s8, 0x3e38aa3b
	s_waitcnt vmcnt(0)
	v_mov_b32_e32 v109, v96
	v_mov_b32_e32 v96, v95
	v_mov_b32_e32 v95, v106
	v_mov_b32_e32 v106, v105
	v_mov_b32_e32 v108, v94
	v_mov_b32_e32 v94, v104
	v_mul_f32_e32 v104, v86, v96
	v_mul_f32_e32 v105, v87, v97
	v_mul_f32_e32 v96, v82, v96
	v_mul_f32_e32 v97, v83, v97
	v_mul_f32_e32 v110, v88, v106
	v_mul_f32_e32 v111, v89, v107
	v_mul_f32_e32 v106, v84, v106
	v_mul_f32_e32 v107, v85, v107
	v_fma_f32 v82, v82, v108, v104
	v_fma_f32 v83, v83, v109, v105
	v_fma_f32 v86, v86, v108, -v96
	v_fma_f32 v87, v87, v109, -v97
	v_fma_f32 v84, v84, v94, v110
	v_fma_f32 v85, v85, v95, v111
	v_fma_f32 v88, v88, v94, -v106
	v_fma_f32 v89, v89, v95, -v107
	s_cmp_lg_u64 s[2:3], 0
	s_cbranch_scc0 .Lqs_skip_1
	v_mul_f32_e32 v86, s8, v86
	v_mul_f32_e32 v87, s8, v87
	v_mul_f32_e32 v88, s8, v88
	v_mul_f32_e32 v89, s8, v89
	v_mul_f32_e32 v82, s8, v82
	v_mul_f32_e32 v83, s8, v83
	v_mul_f32_e32 v84, s8, v84
	v_mul_f32_e32 v85, s8, v85
.Lqs_skip_1:
.LBB2_19:
	v_cvt_pk_f16_f32 v89, v88, v89
	v_cvt_pk_f16_f32 v88, v86, v87
	v_cvt_pk_f16_f32 v85, v84, v85
	v_cvt_pk_f16_f32 v84, v82, v83
	v_add_u32_e32 v82, 0x1800, v92
	ds_write2_b64 v82, v[88:89], v[84:85] offset0:32 offset1:40
	v_or_b32_e32 v82, 32, v103
	v_or_b32_e32 v82, s12, v82
	s_and_b64 vcc, exec, s[4:5]
	v_ashrrev_i32_e32 v83, 31, v82
	s_cbranch_vccnz .LBB2_21
	v_lshlrev_b64 v[84:85], 8, v[82:83]
	v_lshl_add_u64 v[88:89], v[100:101], 0, v[84:85]
	global_load_dwordx4 v[84:87], v[88:89], off
	global_load_dwordx4 v[94:97], v[88:89], off offset:16
	s_mov_b32 s8, 0x3e38aa3b
	s_waitcnt vmcnt(0)
	v_mov_b32_e32 v89, v86
	v_mov_b32_e32 v86, v85
	v_mov_b32_e32 v85, v96
	v_mov_b32_e32 v96, v95
	v_mov_b32_e32 v88, v84
	v_mov_b32_e32 v84, v94
	v_mul_f32_e32 v94, v78, v86
	v_mul_f32_e32 v95, v79, v87
	v_mul_f32_e32 v86, v74, v86
	v_mul_f32_e32 v87, v75, v87
	v_mul_f32_e32 v104, v80, v96
	v_mul_f32_e32 v105, v81, v97
	v_mul_f32_e32 v96, v76, v96
	v_mul_f32_e32 v97, v77, v97
	v_fma_f32 v74, v74, v88, v94
	v_fma_f32 v75, v75, v89, v95
	v_fma_f32 v78, v78, v88, -v86
	v_fma_f32 v79, v79, v89, -v87
	v_fma_f32 v76, v76, v84, v104
	v_fma_f32 v77, v77, v85, v105
	v_fma_f32 v80, v80, v84, -v96
	v_fma_f32 v81, v81, v85, -v97
	s_cmp_lg_u64 s[2:3], 0
	s_cbranch_scc0 .Lqs_skip_2
	v_mul_f32_e32 v78, s8, v78
	v_mul_f32_e32 v79, s8, v79
	v_mul_f32_e32 v80, s8, v80
	v_mul_f32_e32 v81, s8, v81
	v_mul_f32_e32 v74, s8, v74
	v_mul_f32_e32 v75, s8, v75
	v_mul_f32_e32 v76, s8, v76
	v_mul_f32_e32 v77, s8, v77
.Lqs_skip_2:
.LBB2_21:
	v_cvt_pk_f16_f32 v81, v80, v81
	v_cvt_pk_f16_f32 v80, v78, v79
	v_cvt_pk_f16_f32 v77, v76, v77
	v_cvt_pk_f16_f32 v76, v74, v75
	v_add_u32_e32 v74, 0x3000, v92
	ds_write2_b64 v74, v[80:81], v[76:77] offset0:64 offset1:72
	v_or_b32_e32 v74, 48, v103
	v_or_b32_e32 v74, s12, v74
	s_and_b64 vcc, exec, s[4:5]
	v_ashrrev_i32_e32 v75, 31, v74
	s_cbranch_vccnz .LBB2_23
	v_lshlrev_b64 v[76:77], 8, v[74:75]
	v_lshl_add_u64 v[80:81], v[100:101], 0, v[76:77]
	global_load_dwordx4 v[76:79], v[80:81], off
	global_load_dwordx4 v[84:87], v[80:81], off offset:16
	s_mov_b32 s4, 0x3e38aa3b
	s_waitcnt vmcnt(0)
	v_mov_b32_e32 v81, v78
	v_mov_b32_e32 v78, v77
	v_mov_b32_e32 v77, v86
	v_mov_b32_e32 v86, v85
	v_mov_b32_e32 v80, v76
	v_mov_b32_e32 v76, v84
	v_mul_f32_e32 v84, v70, v78
	v_mul_f32_e32 v85, v71, v79
	v_mul_f32_e32 v78, v66, v78
	v_mul_f32_e32 v79, v67, v79
	v_mul_f32_e32 v88, v72, v86
	v_mul_f32_e32 v89, v73, v87
	v_mul_f32_e32 v86, v68, v86
	v_mul_f32_e32 v87, v69, v87
	v_fma_f32 v66, v66, v80, v84
	v_fma_f32 v67, v67, v81, v85
	v_fma_f32 v70, v70, v80, -v78
	v_fma_f32 v71, v71, v81, -v79
	v_fma_f32 v68, v68, v76, v88
	v_fma_f32 v69, v69, v77, v89
	v_fma_f32 v72, v72, v76, -v86
	v_fma_f32 v73, v73, v77, -v87
	s_cmp_lg_u64 s[2:3], 0
	s_cbranch_scc0 .Lqs_skip_3
	v_mul_f32_e32 v70, s4, v70
	v_mul_f32_e32 v71, s4, v71
	v_mul_f32_e32 v72, s4, v72
	v_mul_f32_e32 v73, s4, v73
	v_mul_f32_e32 v66, s4, v66
	v_mul_f32_e32 v67, s4, v67
	v_mul_f32_e32 v68, s4, v68
	v_mul_f32_e32 v69, s4, v69
.Lqs_skip_3:
.LBB2_23:
	s_add_i32 s2, s10, 1
	s_lshr_b32 s4, s2, 1
	v_cvt_pk_f16_f32 v73, v72, v73
	v_cvt_pk_f16_f32 v72, v70, v71
	v_cvt_pk_f16_f32 v69, v68, v69
	v_cvt_pk_f16_f32 v68, v66, v67
	v_add_u32_e32 v66, 0x4800, v92
	s_add_i32 s5, s4, s15
	s_lshl_b32 s2, s2, 4
	ds_write2_b64 v66, v[72:73], v[68:69] offset0:96 offset1:104
	v_and_or_b32 v68, s2, 16, v102
	s_cmp_lt_u32 s5, 32
	s_cselect_b64 s[8:9], -1, 0
	s_cmp_lt_u32 s5, 16
	v_lshlrev_b32_e32 v66, 3, v68
	v_mov_b32_e32 v67, 0
	s_cselect_b64 s[2:3], -1, 0
	s_cmp_gt_u32 s5, 31
	v_lshl_add_u64 v[66:67], s[6:7], 0, v[66:67]
	s_cbranch_scc1 .LBB2_25
	v_lshlrev_b64 v[70:71], 8, v[98:99]
	v_lshl_add_u64 v[76:77], v[66:67], 0, v[70:71]
	global_load_dwordx4 v[70:73], v[76:77], off
	s_nop 0
	global_load_dwordx4 v[76:79], v[76:77], off offset:16
	s_mov_b32 s14, 0x3e38aa3b
	s_waitcnt vmcnt(0)
	v_mov_b32_e32 v81, v72
	v_mov_b32_e32 v72, v71
	v_mov_b32_e32 v71, v78
	v_mov_b32_e32 v78, v77
	v_mov_b32_e32 v80, v70
	v_mov_b32_e32 v70, v76
	v_mul_f32_e32 v76, v62, v72
	v_mul_f32_e32 v77, v63, v73
	v_mul_f32_e32 v72, v58, v72
	v_mul_f32_e32 v73, v59, v73
	v_mul_f32_e32 v84, v64, v78
	v_mul_f32_e32 v85, v65, v79
	v_mul_f32_e32 v78, v60, v78
	v_mul_f32_e32 v79, v61, v79
	v_fma_f32 v58, v58, v80, v76
	v_fma_f32 v59, v59, v81, v77
	v_fma_f32 v62, v62, v80, -v72
	v_fma_f32 v63, v63, v81, -v73
	v_fma_f32 v60, v60, v70, v84
	v_fma_f32 v61, v61, v71, v85
	v_fma_f32 v64, v64, v70, -v78
	v_fma_f32 v65, v65, v71, -v79
	s_cmp_lg_u64 s[2:3], 0
	s_cbranch_scc0 .Lqs_skip_4
	v_mul_f32_e32 v62, s14, v62
	v_mul_f32_e32 v63, s14, v63
	v_mul_f32_e32 v64, s14, v64
	v_mul_f32_e32 v65, s14, v65
	v_mul_f32_e32 v58, s14, v58
	v_mul_f32_e32 v59, s14, v59
	v_mul_f32_e32 v60, s14, v60
	v_mul_f32_e32 v61, s14, v61
.Lqs_skip_4:
.LBB2_25:
	s_lshl_b32 s4, s4, 7
	s_add_i32 s4, s4, 0
	v_lshl_add_u32 v68, v68, 1, s4
	v_cvt_pk_f16_f32 v61, v60, v61
	v_cvt_pk_f16_f32 v60, v58, v59
	v_cndmask_b32_e64 v59, 0, 1, s[8:9]
	v_cvt_pk_f16_f32 v65, v64, v65
	v_cvt_pk_f16_f32 v64, v62, v63
	v_add_u32_e32 v58, v68, v1
	v_cmp_ne_u32_e64 s[4:5], 1, v59
	s_andn2_b64 vcc, exec, s[8:9]
	ds_write2_b64 v58, v[64:65], v[60:61] offset1:8
	s_cbranch_vccnz .LBB2_27
	v_lshlrev_b64 v[60:61], 8, v[90:91]
	v_lshl_add_u64 v[64:65], v[66:67], 0, v[60:61]
	global_load_dwordx4 v[60:63], v[64:65], off
	global_load_dwordx4 v[68:71], v[64:65], off offset:16
	s_mov_b32 s8, 0x3e38aa3b
	s_waitcnt vmcnt(0)
	v_mov_b32_e32 v65, v62
	v_mov_b32_e32 v62, v61
	v_mov_b32_e32 v61, v70
	v_mov_b32_e32 v70, v69
	v_mov_b32_e32 v64, v60
	v_mov_b32_e32 v60, v68
	v_mul_f32_e32 v68, v54, v62
	v_mul_f32_e32 v69, v55, v63
	v_mul_f32_e32 v62, v50, v62
	v_mul_f32_e32 v63, v51, v63
	v_mul_f32_e32 v72, v56, v70
	v_mul_f32_e32 v73, v57, v71
	v_mul_f32_e32 v70, v52, v70
	v_mul_f32_e32 v71, v53, v71
	v_fma_f32 v50, v50, v64, v68
	v_fma_f32 v51, v51, v65, v69
	v_fma_f32 v54, v54, v64, -v62
	v_fma_f32 v55, v55, v65, -v63
	v_fma_f32 v52, v52, v60, v72
	v_fma_f32 v53, v53, v61, v73
	v_fma_f32 v56, v56, v60, -v70
	v_fma_f32 v57, v57, v61, -v71
	s_cmp_lg_u64 s[2:3], 0
	s_cbranch_scc0 .Lqs_skip_5
	v_mul_f32_e32 v54, s8, v54
	v_mul_f32_e32 v55, s8, v55
	v_mul_f32_e32 v56, s8, v56
	v_mul_f32_e32 v57, s8, v57
	v_mul_f32_e32 v50, s8, v50
	v_mul_f32_e32 v51, s8, v51
	v_mul_f32_e32 v52, s8, v52
	v_mul_f32_e32 v53, s8, v53
.Lqs_skip_5:
.LBB2_27:
	v_cvt_pk_f16_f32 v57, v56, v57
	v_cvt_pk_f16_f32 v56, v54, v55
	v_cvt_pk_f16_f32 v53, v52, v53
	v_cvt_pk_f16_f32 v52, v50, v51
	v_add_u32_e32 v50, 0x1800, v58
	s_and_b64 vcc, exec, s[4:5]
	ds_write2_b64 v50, v[56:57], v[52:53] offset0:32 offset1:40
	s_cbranch_vccnz .LBB2_29
	v_lshlrev_b64 v[50:51], 8, v[82:83]
	v_lshl_add_u64 v[60:61], v[66:67], 0, v[50:51]
	global_load_dwordx4 v[50:53], v[60:61], off
	global_load_dwordx4 v[54:57], v[60:61], off offset:16
	s_mov_b32 s8, 0x3e38aa3b
	s_waitcnt vmcnt(0)
	v_mov_b32_e32 v61, v52
	v_mov_b32_e32 v52, v51
	v_mov_b32_e32 v51, v56
	v_mov_b32_e32 v56, v55
	v_mov_b32_e32 v60, v50
	v_mov_b32_e32 v50, v54
	v_mul_f32_e32 v54, v46, v52
	v_mul_f32_e32 v55, v47, v53
	v_mul_f32_e32 v52, v42, v52
	v_mul_f32_e32 v53, v43, v53
	v_mul_f32_e32 v62, v48, v56
	v_mul_f32_e32 v63, v49, v57
	v_mul_f32_e32 v56, v44, v56
	v_mul_f32_e32 v57, v45, v57
	v_fma_f32 v42, v42, v60, v54
	v_fma_f32 v43, v43, v61, v55
	v_fma_f32 v46, v46, v60, -v52
	v_fma_f32 v47, v47, v61, -v53
	v_fma_f32 v44, v44, v50, v62
	v_fma_f32 v45, v45, v51, v63
	v_fma_f32 v48, v48, v50, -v56
	v_fma_f32 v49, v49, v51, -v57
	s_cmp_lg_u64 s[2:3], 0
	s_cbranch_scc0 .Lqs_skip_6
	v_mul_f32_e32 v46, s8, v46
	v_mul_f32_e32 v47, s8, v47
	v_mul_f32_e32 v48, s8, v48
	v_mul_f32_e32 v49, s8, v49
	v_mul_f32_e32 v42, s8, v42
	v_mul_f32_e32 v43, s8, v43
	v_mul_f32_e32 v44, s8, v44
	v_mul_f32_e32 v45, s8, v45
.Lqs_skip_6:
.LBB2_29:
	v_cvt_pk_f16_f32 v49, v48, v49
	v_cvt_pk_f16_f32 v48, v46, v47
	v_cvt_pk_f16_f32 v45, v44, v45
	v_cvt_pk_f16_f32 v44, v42, v43
	v_add_u32_e32 v42, 0x3000, v58
	s_and_b64 vcc, exec, s[4:5]
	ds_write2_b64 v42, v[48:49], v[44:45] offset0:64 offset1:72
	s_cbranch_vccnz .LBB2_31
	v_lshlrev_b64 v[42:43], 8, v[74:75]
	v_lshl_add_u64 v[50:51], v[66:67], 0, v[42:43]
	global_load_dwordx4 v[42:45], v[50:51], off
	global_load_dwordx4 v[46:49], v[50:51], off offset:16
	s_mov_b32 s4, 0x3e38aa3b
	s_waitcnt vmcnt(0)
	v_mov_b32_e32 v51, v44
	v_mov_b32_e32 v44, v43
	v_mov_b32_e32 v43, v48
	v_mov_b32_e32 v48, v47
	v_mov_b32_e32 v50, v42
	v_mov_b32_e32 v42, v46
	v_mul_f32_e32 v46, v38, v44
	v_mul_f32_e32 v47, v39, v45
	v_mul_f32_e32 v44, v34, v44
	v_mul_f32_e32 v45, v35, v45
	v_mul_f32_e32 v52, v40, v48
	v_mul_f32_e32 v53, v41, v49
	v_mul_f32_e32 v48, v36, v48
	v_mul_f32_e32 v49, v37, v49
	v_fma_f32 v34, v34, v50, v46
	v_fma_f32 v35, v35, v51, v47
	v_fma_f32 v38, v38, v50, -v44
	v_fma_f32 v39, v39, v51, -v45
	v_fma_f32 v36, v36, v42, v52
	v_fma_f32 v37, v37, v43, v53
	v_fma_f32 v40, v40, v42, -v48
	v_fma_f32 v41, v41, v43, -v49
	s_cmp_lg_u64 s[2:3], 0
	s_cbranch_scc0 .Lqs_skip_7
	v_mul_f32_e32 v38, s4, v38
	v_mul_f32_e32 v39, s4, v39
	v_mul_f32_e32 v40, s4, v40
	v_mul_f32_e32 v41, s4, v41
	v_mul_f32_e32 v34, s4, v34
	v_mul_f32_e32 v35, s4, v35
	v_mul_f32_e32 v36, s4, v36
	v_mul_f32_e32 v37, s4, v37
.Lqs_skip_7:
.LBB2_31:
	s_add_i32 s10, s10, 2
	s_lshr_b32 s4, s10, 1
	v_cvt_pk_f16_f32 v41, v40, v41
	v_cvt_pk_f16_f32 v40, v38, v39
	v_cvt_pk_f16_f32 v37, v36, v37
	v_cvt_pk_f16_f32 v36, v34, v35
	v_add_u32_e32 v34, 0x4800, v58
	s_add_i32 s5, s4, s15
	s_lshl_b32 s2, s10, 4
	ds_write2_b64 v34, v[40:41], v[36:37] offset0:96 offset1:104
	v_and_or_b32 v36, s2, 16, v102
	s_cmp_lt_u32 s5, 32
	s_cselect_b64 s[8:9], -1, 0
	s_cmp_lt_u32 s5, 16
	v_lshlrev_b32_e32 v34, 3, v36
	v_mov_b32_e32 v35, 0
	s_cselect_b64 s[2:3], -1, 0
	s_cmp_gt_u32 s5, 31
	v_lshl_add_u64 v[34:35], s[6:7], 0, v[34:35]
	s_cbranch_scc1 .LBB2_33
	v_lshlrev_b64 v[38:39], 8, v[98:99]
	v_lshl_add_u64 v[46:47], v[34:35], 0, v[38:39]
	global_load_dwordx4 v[38:41], v[46:47], off
	global_load_dwordx4 v[42:45], v[46:47], off offset:16
	s_mov_b32 s6, 0x3e38aa3b
	s_waitcnt vmcnt(0)
	v_mov_b32_e32 v47, v40
	v_mov_b32_e32 v40, v39
	v_mov_b32_e32 v39, v44
	v_mov_b32_e32 v44, v43
	v_mov_b32_e32 v46, v38
	v_mov_b32_e32 v38, v42
	v_mul_f32_e32 v42, v30, v40
	v_mul_f32_e32 v43, v31, v41
	v_mul_f32_e32 v40, v26, v40
	v_mul_f32_e32 v41, v27, v41
	v_mul_f32_e32 v48, v32, v44
	v_mul_f32_e32 v49, v33, v45
	v_mul_f32_e32 v44, v28, v44
	v_mul_f32_e32 v45, v29, v45
	v_fma_f32 v26, v26, v46, v42
	v_fma_f32 v27, v27, v47, v43
	v_fma_f32 v30, v30, v46, -v40
	v_fma_f32 v31, v31, v47, -v41
	v_fma_f32 v28, v28, v38, v48
	v_fma_f32 v29, v29, v39, v49
	v_fma_f32 v32, v32, v38, -v44
	v_fma_f32 v33, v33, v39, -v45
	s_cmp_lg_u64 s[2:3], 0
	s_cbranch_scc0 .Lqs_skip_8
	v_mul_f32_e32 v30, s6, v30
	v_mul_f32_e32 v31, s6, v31
	v_mul_f32_e32 v32, s6, v32
	v_mul_f32_e32 v33, s6, v33
	v_mul_f32_e32 v26, s6, v26
	v_mul_f32_e32 v27, s6, v27
	v_mul_f32_e32 v28, s6, v28
	v_mul_f32_e32 v29, s6, v29
.Lqs_skip_8:
.LBB2_33:
	s_lshl_b32 s4, s4, 7
	s_add_i32 s4, s4, 0
	v_lshl_add_u32 v36, v36, 1, s4
	v_cvt_pk_f16_f32 v29, v28, v29
	v_cvt_pk_f16_f32 v28, v26, v27
	v_cndmask_b32_e64 v26, 0, 1, s[8:9]
	v_cvt_pk_f16_f32 v33, v32, v33
	v_cvt_pk_f16_f32 v32, v30, v31
	v_add_u32_e32 v1, v36, v1
	v_cmp_ne_u32_e64 s[4:5], 1, v26
	s_andn2_b64 vcc, exec, s[8:9]
	ds_write2_b64 v1, v[32:33], v[28:29] offset1:8
	s_cbranch_vccnz .LBB2_35
	v_lshlrev_b64 v[26:27], 8, v[90:91]
	v_lshl_add_u64 v[36:37], v[34:35], 0, v[26:27]
	global_load_dwordx4 v[26:29], v[36:37], off
	global_load_dwordx4 v[30:33], v[36:37], off offset:16
	s_mov_b32 s6, 0x3e38aa3b
	s_waitcnt vmcnt(0)
	v_mov_b32_e32 v37, v28
	v_mov_b32_e32 v28, v27
	v_mov_b32_e32 v27, v32
	v_mov_b32_e32 v32, v31
	v_mov_b32_e32 v36, v26
	v_mov_b32_e32 v26, v30
	v_mul_f32_e32 v30, v22, v28
	v_mul_f32_e32 v31, v23, v29
	v_mul_f32_e32 v28, v18, v28
	v_mul_f32_e32 v29, v19, v29
	v_mul_f32_e32 v38, v24, v32
	v_mul_f32_e32 v39, v25, v33
	v_mul_f32_e32 v32, v20, v32
	v_mul_f32_e32 v33, v21, v33
	v_fma_f32 v18, v18, v36, v30
	v_fma_f32 v19, v19, v37, v31
	v_fma_f32 v22, v22, v36, -v28
	v_fma_f32 v23, v23, v37, -v29
	v_fma_f32 v20, v20, v26, v38
	v_fma_f32 v21, v21, v27, v39
	v_fma_f32 v24, v24, v26, -v32
	v_fma_f32 v25, v25, v27, -v33
	s_cmp_lg_u64 s[2:3], 0
	s_cbranch_scc0 .Lqs_skip_9
	v_mul_f32_e32 v22, s6, v22
	v_mul_f32_e32 v23, s6, v23
	v_mul_f32_e32 v24, s6, v24
	v_mul_f32_e32 v25, s6, v25
	v_mul_f32_e32 v18, s6, v18
	v_mul_f32_e32 v19, s6, v19
	v_mul_f32_e32 v20, s6, v20
	v_mul_f32_e32 v21, s6, v21
.Lqs_skip_9:
.LBB2_35:
	v_cvt_pk_f16_f32 v25, v24, v25
	v_cvt_pk_f16_f32 v24, v22, v23
	v_cvt_pk_f16_f32 v21, v20, v21
	v_cvt_pk_f16_f32 v20, v18, v19
	v_add_u32_e32 v18, 0x1800, v1
	s_and_b64 vcc, exec, s[4:5]
	ds_write2_b64 v18, v[24:25], v[20:21] offset0:32 offset1:40
	s_cbranch_vccnz .LBB2_37
	v_lshlrev_b64 v[18:19], 8, v[82:83]
	v_lshl_add_u64 v[26:27], v[34:35], 0, v[18:19]
	global_load_dwordx4 v[18:21], v[26:27], off
	global_load_dwordx4 v[22:25], v[26:27], off offset:16
	s_mov_b32 s6, 0x3e38aa3b
	s_waitcnt vmcnt(0)
	v_mov_b32_e32 v27, v20
	v_mov_b32_e32 v20, v19
	v_mov_b32_e32 v19, v24
	v_mov_b32_e32 v24, v23
	v_mov_b32_e32 v26, v18
	v_mov_b32_e32 v18, v22
	v_mul_f32_e32 v22, v14, v20
	v_mul_f32_e32 v23, v15, v21
	v_mul_f32_e32 v20, v10, v20
	v_mul_f32_e32 v21, v11, v21
	v_mul_f32_e32 v28, v16, v24
	v_mul_f32_e32 v29, v17, v25
	v_mul_f32_e32 v24, v12, v24
	v_mul_f32_e32 v25, v13, v25
	v_fma_f32 v10, v10, v26, v22
	v_fma_f32 v11, v11, v27, v23
	v_fma_f32 v14, v14, v26, -v20
	v_fma_f32 v15, v15, v27, -v21
	v_fma_f32 v12, v12, v18, v28
	v_fma_f32 v13, v13, v19, v29
	v_fma_f32 v16, v16, v18, -v24
	v_fma_f32 v17, v17, v19, -v25
	s_cmp_lg_u64 s[2:3], 0
	s_cbranch_scc0 .Lqs_skip_10
	v_mul_f32_e32 v14, s6, v14
	v_mul_f32_e32 v15, s6, v15
	v_mul_f32_e32 v16, s6, v16
	v_mul_f32_e32 v17, s6, v17
	v_mul_f32_e32 v10, s6, v10
	v_mul_f32_e32 v11, s6, v11
	v_mul_f32_e32 v12, s6, v12
	v_mul_f32_e32 v13, s6, v13
.Lqs_skip_10:
.LBB2_37:
	v_cvt_pk_f16_f32 v17, v16, v17
	v_cvt_pk_f16_f32 v16, v14, v15
	v_cvt_pk_f16_f32 v13, v12, v13
	v_cvt_pk_f16_f32 v12, v10, v11
	v_add_u32_e32 v10, 0x3000, v1
	s_and_b64 vcc, exec, s[4:5]
	ds_write2_b64 v10, v[16:17], v[12:13] offset0:64 offset1:72
	s_cbranch_vccnz .LBB2_39
	v_lshlrev_b64 v[10:11], 8, v[74:75]
	v_lshl_add_u64 v[18:19], v[34:35], 0, v[10:11]
	global_load_dwordx4 v[10:13], v[18:19], off
	global_load_dwordx4 v[14:17], v[18:19], off offset:16
	s_mov_b32 s4, 0x3e38aa3b
	s_waitcnt vmcnt(0)
	v_mov_b32_e32 v19, v12
	v_mov_b32_e32 v12, v11
	v_mov_b32_e32 v11, v16
	v_mov_b32_e32 v16, v15
	v_mov_b32_e32 v18, v10
	v_mov_b32_e32 v10, v14
	v_mul_f32_e32 v14, v6, v12
	v_mul_f32_e32 v15, v7, v13
	v_mul_f32_e32 v12, v2, v12
	v_mul_f32_e32 v13, v3, v13
	v_mul_f32_e32 v20, v8, v16
	v_mul_f32_e32 v21, v9, v17
	v_mul_f32_e32 v16, v4, v16
	v_mul_f32_e32 v17, v5, v17
	v_fma_f32 v2, v2, v18, v14
	v_fma_f32 v3, v3, v19, v15
	v_fma_f32 v6, v6, v18, -v12
	v_fma_f32 v7, v7, v19, -v13
	v_fma_f32 v4, v4, v10, v20
	v_fma_f32 v5, v5, v11, v21
	v_fma_f32 v8, v8, v10, -v16
	v_fma_f32 v9, v9, v11, -v17
	s_cmp_lg_u64 s[2:3], 0
	s_cbranch_scc0 .Lqs_skip_11
	v_mul_f32_e32 v6, s4, v6
	v_mul_f32_e32 v7, s4, v7
	v_mul_f32_e32 v8, s4, v8
	v_mul_f32_e32 v9, s4, v9
	v_mul_f32_e32 v2, s4, v2
	v_mul_f32_e32 v3, s4, v3
	v_mul_f32_e32 v4, s4, v4
	v_mul_f32_e32 v5, s4, v5
